# stack B plus: SB/MEM work-queue pop for the next unit issued at the start of the current unit and consumed at the next loop top
# speedup vs baseline: 1.0013x; 1.0013x over previous
.LBB0_785:
	s_mov_b32 s100, 0
	v_and_b32_e32 v174, 0x78, v214
	v_lshrrev_b32_e32 v171, 4, v0
	v_lshrrev_b32_e32 v1, 3, v0
	v_lshlrev_b32_e32 v173, 1, v174
	s_movk_i32 s1, 0x70
	v_writelane_b32 v255, s91, 1
	v_and_b32_e32 v1, 8, v1
	v_or_b32_e32 v187, 32, v171
	v_bitop3_b32 v149, v173, v0, s1 bitop3:0x78
	s_movk_i32 s1, 0x60
	v_writelane_b32 v254, s88, 63
	s_add_u32 s78, s92, 0x3c100
	v_and_or_b32 v2, v171, 16, v1
	v_writelane_b32 v255, s89, 0
	v_lshrrev_b32_e32 v3, 5, v0
	s_waitcnt vmcnt(9)
	v_bfe_u32 v5, v0, 4, 2
	v_and_or_b32 v1, v187, 48, v1
	v_bitop3_b32 v161, v183, v186, s1 bitop3:0x36
	s_movk_i32 s1, 0x80
	v_writelane_b32 v255, s85, 3
	s_addc_u32 s79, s93, 0
	s_add_i32 s0, 0, 0x8000
	v_lshrrev_b32_e32 v2, 1, v2
	v_bfe_u32 v4, v214, 5, 2
	v_and_or_b32 v5, v3, 4, v5
	v_lshrrev_b32_e32 v1, 1, v1
	v_bitop3_b32 v163, v183, v186, s1 bitop3:0x36
	s_movk_i32 s1, 0xa0
	v_add_u32_e32 v145, s0, v220
	v_or_b32_e32 v2, v2, v4
	v_or_b32_e32 v1, v1, v4
	s_movk_i32 s0, 0xe0
	v_lshlrev_b32_e32 v4, 8, v171
	v_add_u32_e32 v6, 0, v149
	v_lshlrev_b32_e32 v7, 8, v187
	v_lshl_add_u32 v5, v5, 6, 0
	v_bitop3_b32 v165, v183, v186, s1 bitop3:0x36
	s_movk_i32 s1, 0xc0
	v_writelane_b32 v255, s96, 5
	s_mov_b32 s89, 0
	v_and_b32_e32 v147, 48, v173
	v_mov_b32_e32 v3, 0
	v_or_b32_e32 v192, 0xe0, v171
	v_and_b32_e32 v175, 0x70, v0
	v_lshl_add_u32 v151, v2, 9, v5
	v_lshl_add_u32 v153, v1, 9, v5
	v_xor_b32_e32 v155, v183, v186
	v_bitop3_b32 v157, v183, v186, 32 bitop3:0x36
	v_bitop3_b32 v159, v183, v186, 64 bitop3:0x36
	v_bitop3_b32 v167, v183, v186, s1 bitop3:0x36
	v_bitop3_b32 v169, v183, v186, s0 bitop3:0x36
	v_cmp_eq_u32_e64 s[4:5], 0, v213
	v_cmp_eq_u32_e64 s[6:7], 0, v251
	v_or_b32_e32 v144, 8, v184
	v_or_b32_e32 v146, 16, v184
	v_or_b32_e32 v148, 24, v184
	v_or_b32_e32 v150, 1, v184
	v_or_b32_e32 v152, 2, v184
	v_or_b32_e32 v154, 3, v184
	v_or_b32_e32 v156, 9, v184
	v_or_b32_e32 v158, 10, v184
	v_or_b32_e32 v160, 11, v184
	v_or_b32_e32 v162, 17, v184
	v_or_b32_e32 v164, 18, v184
	v_or_b32_e32 v166, 19, v184
	v_or_b32_e32 v168, 25, v184
	v_or_b32_e32 v170, 26, v184
	v_or_b32_e32 v172, 27, v184
	v_or_b32_e32 v193, 0xc0, v171
	s_add_i32 s91, 0, 0x20500
	s_movk_i32 s33, 0x6880
	v_add_u32_e32 v194, v6, v4
	v_add_u32_e32 v195, v6, v7
	s_movk_i32 s76, 0x1880
	v_mov_b32_e32 v196, 0x1880
	v_writelane_b32 v255, s97, 6
	s_branch .LBB0_788

.LBB0_788:
	s_barrier
	s_mov_b64 s[0:1], exec
	v_readlane_b32 s2, v254, 29
	v_readlane_b32 s3, v254, 30
	s_and_b64 s[2:3], s[0:1], s[2:3]
	s_mov_b64 exec, s[2:3]
	s_cbranch_execz .LBB0_792
	s_mov_b64 s[10:11], exec
	v_mbcnt_lo_u32_b32 v1, s10, 0
	v_mbcnt_hi_u32_b32 v2, s11, v1
	v_cmp_eq_u32_e32 vcc, 0, v2
	s_and_saveexec_b64 s[8:9], vcc
	s_cbranch_execz .LBB0_791
	s_cmp_lg_u32 s100, 0
	s_cbranch_scc1 .Lsbq_have
	s_bcnt1_i32_b64 s2, s[10:11]
	v_mov_b32_e32 v1, s2
	global_atomic_add v4, v3, v1, s[78:79] sc0
	s_branch .LBB0_791
.Lsbq_have:
	s_waitcnt vmcnt(0)
	v_mov_b32_e32 v4, v252

.LBB0_792:
	s_or_b64 exec, exec, s[0:1]
	v_mov_b32_e32 v1, s91
	s_waitcnt lgkmcnt(0)
	s_barrier
	ds_read_b32 v1, v1
	s_movk_i32 s0, 0x1ff
	s_waitcnt lgkmcnt(0)
	v_cmp_lt_i32_e32 vcc, s0, v1
	v_readfirstlane_b32 s2, v1
	s_mov_b64 s[0:1], -1
	s_cbranch_vccnz .LBB0_787
	s_mov_b64 s[20:21], exec
	v_readlane_b32 s22, v254, 29
	v_readlane_b32 s23, v254, 30
	s_and_b64 s[22:23], s[20:21], s[22:23]
	s_mov_b64 exec, s[22:23]
	s_cbranch_execz .Lsbq_pfx
	v_mbcnt_lo_u32_b32 v253, s22, 0
	v_mbcnt_hi_u32_b32 v253, s23, v253
	v_cmp_eq_u32_e32 vcc, 0, v253
	s_and_saveexec_b64 s[24:25], vcc
	s_cbranch_execz .Lsbq_pfx
	s_bcnt1_i32_b64 s26, s[22:23]
	v_mov_b32_e32 v253, s26
	global_atomic_add v252, v3, v253, s[78:79] sc0
.Lsbq_pfx:
	s_mov_b64 exec, s[20:21]
	s_mov_b32 s100, 1
	s_ashr_i32 s0, s2, 31
	s_lshr_b32 s0, s0, 28
	s_add_i32 s0, s2, s0
	s_lshr_b32 s1, s0, 4
	s_and_b32 s0, s0, -16
	v_readfirstlane_b32 s8, v0
	s_sub_i32 s2, s2, s0
	s_lshr_b32 s12, s8, 6
	s_lshl_b32 s13, s1, 8
	s_sub_i32 s3, 0, s1
	s_ashr_i32 s0, s2, 3
	s_sub_i32 s97, 0x1f00, s13
	s_lshl_b32 s1, s12, 5
	s_mov_b32 s86, s1
	s_add_i32 s14, s1, s97
	s_ashr_i32 s1, s0, 31
	s_lshl_b64 s[18:19], s[0:1], 13
	s_lshl_b32 s1, s2, 7
	s_lshl_b32 s96, s3, 8
	s_and_b32 s3, s1, 0x380
	s_lshl_b32 s88, s3, 1
	s_mul_hi_i32 s1, s0, 0xd100000
	s_mul_i32 s0, s0, 0xd100000
	v_readlane_b32 s16, v254, 63
	v_readlane_b32 s17, v255, 0
	s_add_u32 s0, s16, s0
	s_addc_u32 s1, s17, s1
	s_add_u32 s2, s0, s88
	s_addc_u32 s9, s1, 0
	s_add_u32 s0, s2, 0x2000
	s_addc_u32 s1, s9, 0
	v_or_b32_e32 v1, s97, v193
	v_mov_b64_e32 v[4:5], s[0:1]
	v_mad_u64_u32 v[6:7], s[10:11], v1, s33, v[4:5]
	v_or_b32_e32 v1, s97, v192
	s_add_u32 s8, s2, 0x2800
	v_lshlrev_b32_e32 v2, 1, v174
	v_mad_u64_u32 v[4:5], s[10:11], v1, s33, v[4:5]
	s_addc_u32 s9, s9, 0
	v_lshl_add_u64 v[6:7], v[6:7], 0, v[2:3]
	v_lshl_add_u64 v[4:5], v[4:5], 0, v[2:3]
	s_sub_i32 s2, 0x1fc0, s13
	s_barrier
	global_load_dwordx4 v[100:103], v[6:7], off
	global_load_dwordx4 v[104:107], v[4:5], off
	v_or_b32_e32 v1, s2, v171
	v_mov_b64_e32 v[4:5], s[8:9]
	v_mad_u64_u32 v[6:7], s[10:11], v1, s33, v[4:5]
	v_or_b32_e32 v1, s2, v187
	v_lshl_add_u64 v[6:7], v[6:7], 0, v[2:3]
	v_mad_u64_u32 v[4:5], s[10:11], v1, s33, v[4:5]
	v_lshl_add_u64 v[4:5], v[4:5], 0, v[2:3]
	global_load_dwordx4 v[108:111], v[6:7], off
	global_load_dwordx4 v[112:115], v[4:5], off
	v_or_b32_e32 v176, s14, v180
	v_mov_b32_e32 v177, v3
	v_lshl_add_u64 v[4:5], s[18:19], 0, v[176:177]
	v_mov_b64_e32 v[6:7], s[16:17]
	v_mad_u64_u32 v[6:7], s[10:11], v4, s33, v[6:7]
	v_mad_i32_i24 v7, v5, s33, v7
	v_lshl_add_u64 v[4:5], v[6:7], 0, s[88:89]
	s_mov_b64 s[10:11], 0x1800
	s_waitcnt vmcnt(10)
	v_mov_b32_e32 v16, v3
	v_mov_b32_e32 v17, v3
	v_lshl_add_u64 v[178:179], v[4:5], 0, s[10:11]
	v_lshl_add_u64 v[188:189], s[8:9], 0, v[2:3]
	v_lshl_add_u64 v[190:191], s[0:1], 0, v[2:3]
	v_mov_b32_e32 v2, v3
	v_mov_b32_e32 v4, v3
	v_mov_b32_e32 v5, v3
	v_mov_b32_e32 v6, v3
	v_mov_b32_e32 v7, v3
	v_mov_b32_e32 v8, v3
	v_mov_b32_e32 v9, v3
	v_mov_b32_e32 v10, v3
	v_mov_b32_e32 v11, v3
	v_mov_b32_e32 v12, v3
	v_mov_b32_e32 v13, v3
	v_mov_b32_e32 v14, v3
	v_mov_b32_e32 v15, v3
	s_waitcnt vmcnt(6)
	v_mov_b64_e32 v[66:67], v[16:17]
	v_mov_b64_e32 v[50:51], v[16:17]
	v_mov_b64_e32 v[34:35], v[16:17]
	s_sub_i32 s10, 0x2000, s13
	s_lshl_b32 s0, s12, 2
	v_mov_b64_e32 v[64:65], v[14:15]
	v_mov_b64_e32 v[62:63], v[12:13]
	v_mov_b64_e32 v[60:61], v[10:11]
	v_mov_b64_e32 v[58:59], v[8:9]
	v_mov_b64_e32 v[56:57], v[6:7]
	v_mov_b64_e32 v[54:55], v[4:5]
	v_mov_b64_e32 v[52:53], v[2:3]
	v_mov_b64_e32 v[48:49], v[14:15]
	v_mov_b64_e32 v[46:47], v[12:13]
	v_mov_b64_e32 v[44:45], v[10:11]
	v_mov_b64_e32 v[42:43], v[8:9]
	v_mov_b64_e32 v[40:41], v[6:7]
	v_mov_b64_e32 v[38:39], v[4:5]
	v_mov_b64_e32 v[36:37], v[2:3]
	v_mov_b64_e32 v[32:33], v[14:15]
	v_mov_b64_e32 v[30:31], v[12:13]
	v_mov_b64_e32 v[28:29], v[10:11]
	v_mov_b64_e32 v[26:27], v[8:9]
	v_mov_b64_e32 v[24:25], v[6:7]
	v_mov_b64_e32 v[22:23], v[4:5]
	v_mov_b64_e32 v[20:21], v[2:3]
	v_mov_b64_e32 v[18:19], v[16:17]
	s_mov_b64 s[80:81], s[82:83]
	s_mov_b32 s2, 0
	s_mov_b64 s[82:83], s[18:19]
	s_lshr_b32 s88, s10, 6
	s_add_i32 s77, s0, 0
	v_mov_b32_e32 v198, 1.0
	v_mov_b32_e32 v177, v184
	v_mov_b32_e32 v197, v171
	v_mov_b64_e32 v[16:17], v[14:15]
	v_mov_b64_e32 v[14:15], v[12:13]
	v_mov_b64_e32 v[12:13], v[10:11]
	v_mov_b64_e32 v[10:11], v[8:9]
	v_mov_b64_e32 v[8:9], v[6:7]
	v_mov_b64_e32 v[6:7], v[4:5]
	v_mov_b64_e32 v[4:5], v[2:3]

.LBB0_806:
	s_mov_b32 s101, 0
	s_mov_b64 s[0:1], exec
	v_readlane_b32 s2, v254, 29
	v_readlane_b32 s3, v254, 30
	v_readlane_b32 s80, v254, 63
	v_readlane_b32 s28, v254, 57
	s_and_b64 s[2:3], s[0:1], s[2:3]
	v_readlane_b32 s85, v255, 3
	v_readlane_b32 s81, v255, 0
	v_readlane_b32 s29, v254, 58
	v_readlane_b32 s91, v255, 1
	s_mov_b64 exec, s[2:3]
	s_cbranch_execz .LBB0_816
	s_add_u32 s4, s92, 0x3c300
	s_addc_u32 s5, s93, 0
	s_mov_b32 s2, 0x400001
	v_mov_b32_e32 v2, 0
	s_branch .LBB0_809

.LBB0_819:
	s_barrier
	s_mov_b64 s[12:13], exec
	v_readlane_b32 s14, v254, 29
	v_readlane_b32 s15, v254, 30
	s_and_b64 s[14:15], s[12:13], s[14:15]
	s_mov_b64 exec, s[14:15]
	s_cbranch_execz .LBB0_823
	s_mov_b64 s[16:17], exec
	v_mbcnt_lo_u32_b32 v1, s16, 0
	v_mbcnt_hi_u32_b32 v2, s17, v1
	v_cmp_eq_u32_e32 vcc, 0, v2
	s_and_saveexec_b64 s[14:15], vcc
	s_cbranch_execz .LBB0_822
	s_cmp_lg_u32 s101, 0
	s_cbranch_scc1 .Lmemq_have
	s_bcnt1_i32_b64 s4, s[16:17]
	v_mov_b32_e32 v1, s4
	global_atomic_add v4, v3, v1, s[0:1] sc0
	s_branch .LBB0_822

.LBB0_823:
	s_or_b64 exec, exec, s[12:13]
	s_waitcnt lgkmcnt(0)
	s_barrier
	ds_read_b32 v1, v138
	s_mov_b64 s[12:13], -1
	s_waitcnt lgkmcnt(0)
	v_cmp_lt_i32_e32 vcc, s3, v1
	v_readfirstlane_b32 s4, v1
	s_cbranch_vccnz .LBB0_818
	s_mov_b64 s[12:13], exec
	v_readlane_b32 s14, v254, 29
	v_readlane_b32 s15, v254, 30
	s_and_b64 s[14:15], s[12:13], s[14:15]
	s_mov_b64 exec, s[14:15]
	s_cbranch_execz .Lmemq_pfx
	v_mbcnt_lo_u32_b32 v253, s14, 0
	v_mbcnt_hi_u32_b32 v253, s15, v253
	v_cmp_eq_u32_e32 vcc, 0, v253
	s_and_saveexec_b64 s[16:17], vcc
	s_cbranch_execz .Lmemq_pfx
	s_bcnt1_i32_b64 s22, s[14:15]
	v_mov_b32_e32 v253, s22
	global_atomic_add v252, v3, v253, s[0:1] sc0
.Lmemq_pfx:
	s_mov_b64 exec, s[12:13]
	s_mov_b32 s101, 1
	v_readfirstlane_b32 s12, v0
	s_lshl_b32 s13, s4, 8
	s_ashr_i32 s14, s4, 8
	s_and_b32 s22, s13, 0x1f00
	s_lshr_b32 s13, s12, 1
	s_and_b32 s23, s13, 0x7fffffe0
	s_ashr_i32 s15, s14, 31
	s_add_i32 s26, s23, s22
	s_and_b32 s25, s12, 0x3fffffc0
	s_lshl_b64 s[12:13], s[14:15], 13
	s_lshl_b32 s24, s4, 2
	s_mul_hi_i32 s15, s14, 0x108000
	s_mul_i32 s14, s14, 0x108000
	s_add_u32 s16, s28, s14
	s_addc_u32 s17, s29, s15
	s_lshl_b32 s27, s4, 3
	s_and_b32 s4, s27, 0x600
	s_add_u32 s16, s16, s4
	s_addc_u32 s17, s17, 0
	v_mov_b32_e32 v127, v3
	s_lshl_b32 s25, s25, 2
	v_lshl_add_u64 v[4:5], s[16:17], 0, v[126:127]
	v_mov_b32_e32 v129, v3
	s_add_i32 s25, s25, 0
	s_and_b32 s27, s27, 0x100
	v_lshl_add_u64 v[4:5], v[4:5], 0, v[128:129]
	s_add_u32 s16, s16, s27
	v_add_co_u32_e32 v8, vcc, s19, v4
	s_addc_u32 s17, s17, 0
	s_barrier
	v_lshl_add_u64 v[6:7], v[4:5], 0, s[6:7]
	v_addc_co_u32_e32 v9, vcc, 0, v5, vcc
	global_load_dwordx4 v[100:103], v[4:5], off
	global_load_dwordx4 v[104:107], v[4:5], off offset:256
	global_load_dwordx4 v[108:111], v[8:9], off
	global_load_dwordx4 v[112:115], v[6:7], off offset:256
	v_lshl_add_u64 v[4:5], s[16:17], 0, v[126:127]
	v_lshl_add_u64 v[4:5], v[4:5], 0, v[128:129]
	v_add_co_u32_e32 v6, vcc, s19, v4
	v_or_b32_e32 v2, s26, v180
	s_nop 0
	v_addc_co_u32_e32 v7, vcc, 0, v5, vcc
	global_load_dwordx4 v[116:119], v[4:5], off offset:2048
	global_load_dwordx4 v[120:123], v[6:7], off offset:2048
	v_lshl_add_u64 v[4:5], s[12:13], 0, v[2:3]
	v_mov_b64_e32 v[6:7], s[80:81]
	v_mad_u64_u32 v[6:7], s[16:17], v4, s18, v[6:7]
	v_mad_i32_i24 v7, v5, s18, v7
	v_lshl_add_u64 v[4:5], v[6:7], 0, s[4:5]
	v_mov_b32_e32 v16, v3
	v_mov_b32_e32 v17, v3
	v_lshl_add_u64 v[130:131], v[4:5], 0, s[8:9]
	s_or_b32 s14, s14, s4
	v_mov_b32_e32 v2, v3
	v_mov_b32_e32 v4, v3
	v_mov_b32_e32 v5, v3
	v_mov_b32_e32 v6, v3
	v_mov_b32_e32 v7, v3
	v_mov_b32_e32 v8, v3
	v_mov_b32_e32 v9, v3
	v_mov_b32_e32 v10, v3
	v_mov_b32_e32 v11, v3
	v_mov_b32_e32 v12, v3
	v_mov_b32_e32 v13, v3
	v_mov_b32_e32 v14, v3
	v_mov_b32_e32 v15, v3
	v_mov_b64_e32 v[66:67], v[16:17]
	v_mov_b64_e32 v[50:51], v[16:17]
	v_mov_b64_e32 v[34:35], v[16:17]
	s_or_b32 s16, s14, s27
	s_mov_b32 s17, s15
	v_mov_b64_e32 v[64:65], v[14:15]
	v_mov_b64_e32 v[62:63], v[12:13]
	v_mov_b64_e32 v[60:61], v[10:11]
	v_mov_b64_e32 v[58:59], v[8:9]
	v_mov_b64_e32 v[56:57], v[6:7]
	v_mov_b64_e32 v[54:55], v[4:5]
	v_mov_b64_e32 v[52:53], v[2:3]
	v_mov_b64_e32 v[48:49], v[14:15]
	v_mov_b64_e32 v[46:47], v[12:13]
	v_mov_b64_e32 v[44:45], v[10:11]
	v_mov_b64_e32 v[42:43], v[8:9]
	v_mov_b64_e32 v[40:41], v[6:7]
	v_mov_b64_e32 v[38:39], v[4:5]
	v_mov_b64_e32 v[36:37], v[2:3]
	v_mov_b64_e32 v[32:33], v[14:15]
	v_mov_b64_e32 v[30:31], v[12:13]
	v_mov_b64_e32 v[28:29], v[10:11]
	v_mov_b64_e32 v[26:27], v[8:9]
	v_mov_b64_e32 v[24:25], v[6:7]
	v_mov_b64_e32 v[22:23], v[4:5]
	v_mov_b64_e32 v[20:21], v[2:3]
	v_mov_b64_e32 v[18:19], v[16:17]
	v_lshl_add_u32 v127, v180, 2, s25
	v_lshl_add_u64 v[132:133], v[124:125], 0, s[16:17]
	v_lshl_add_u64 v[134:135], v[124:125], 0, s[14:15]
	v_mov_b32_e32 v129, 0
	v_mov_b32_e32 v179, 0xf149f2ca
	s_mov_b64 s[14:15], 0
	v_mov_b64_e32 v[16:17], v[14:15]
	v_mov_b64_e32 v[14:15], v[12:13]
	v_mov_b64_e32 v[12:13], v[10:11]
	v_mov_b64_e32 v[10:11], v[8:9]
	v_mov_b64_e32 v[8:9], v[6:7]
	v_mov_b64_e32 v[6:7], v[4:5]
	v_mov_b64_e32 v[4:5], v[2:3]
